# baseline (speedup 1.0000x reference)
.Lp1_nomask:
	v_cmp_eq_u32_e32 vcc, 0, v0
	s_and_b64 exec, exec, vcc
	s_cbranch_execz .Lp1_end
	v_mov_b32_e32 v2, 1
	s_and_b32 s3, s2, 63
	s_cmp_lt_u32 s3, 9
	s_cselect_b32 s24, 8, 7
	s_lshl_b32 s3, s3, 6
	s_add_u32 s3, s3, 8
	v_mov_b32_e32 v3, s3
	global_atomic_add v4, v3, v2, s[8:9] sc0
	s_waitcnt vmcnt(0)
	v_readfirstlane_b32 s3, v4
	s_cmp_lg_u32 s3, s24
	s_cbranch_scc1 .Lp1_end
	v_mov_b32_e32 v3, 4
	global_atomic_add v3, v2, s[8:9] offset:0
	global_atomic_add v3, v2, s[8:9] offset:64
	global_atomic_add v3, v2, s[8:9] offset:128
	global_atomic_add v3, v2, s[8:9] offset:192
	global_atomic_add v3, v2, s[8:9] offset:256
	global_atomic_add v3, v2, s[8:9] offset:320
	global_atomic_add v3, v2, s[8:9] offset:384
	global_atomic_add v3, v2, s[8:9] offset:448
	global_atomic_add v3, v2, s[8:9] offset:512
	global_atomic_add v3, v2, s[8:9] offset:576
	global_atomic_add v3, v2, s[8:9] offset:640
	global_atomic_add v3, v2, s[8:9] offset:704
	global_atomic_add v3, v2, s[8:9] offset:768
	global_atomic_add v3, v2, s[8:9] offset:832
	global_atomic_add v3, v2, s[8:9] offset:896
	global_atomic_add v3, v2, s[8:9] offset:960
	global_atomic_add v3, v2, s[8:9] offset:1024
	global_atomic_add v3, v2, s[8:9] offset:1088
	global_atomic_add v3, v2, s[8:9] offset:1152
	global_atomic_add v3, v2, s[8:9] offset:1216
	global_atomic_add v3, v2, s[8:9] offset:1280
	global_atomic_add v3, v2, s[8:9] offset:1344
	global_atomic_add v3, v2, s[8:9] offset:1408
	global_atomic_add v3, v2, s[8:9] offset:1472
	global_atomic_add v3, v2, s[8:9] offset:1536
	global_atomic_add v3, v2, s[8:9] offset:1600
	global_atomic_add v3, v2, s[8:9] offset:1664
	global_atomic_add v3, v2, s[8:9] offset:1728
	global_atomic_add v3, v2, s[8:9] offset:1792
	global_atomic_add v3, v2, s[8:9] offset:1856
	global_atomic_add v3, v2, s[8:9] offset:1920
	global_atomic_add v3, v2, s[8:9] offset:1984

.Lp2_entry:
	s_load_dwordx2 s[4:5], s[0:1], 0x10
	s_load_dwordx2 s[6:7], s[0:1], 0x18
	s_load_dwordx2 s[10:11], s[0:1], 0x28
	s_load_dwordx4 s[16:19], s[0:1], 0x30
	s_load_dwordx2 s[20:21], s[0:1], 0x40
	s_load_dwordx2 s[12:13], s[0:1], 0x50
	s_load_dwordx2 s[8:9], s[0:1], 0x20
	s_sub_i32 s33, s2, 521
	s_mov_b32 s30, 0xc350
	v_lshlrev_b32_e32 v1, 3, v0
	v_mov_b32_e32 v2, 0
	v_mov_b32_e32 v3, 0
	ds_write_b64 v1, v[2:3]
	ds_write_b64 v1, v[2:3] offset:1024
	ds_write_b64 v1, v[2:3] offset:2048
	v_mov_b32_e32 v12, 1
	v_mov_b32_e32 v19, 0
	s_mov_b64 s[38:39], 0
	v_mov_b32_e32 v18, 0x400
	s_waitcnt lgkmcnt(0)
	s_lshl_b32 s35, s33, 2
	s_add_u32 s24, s12, 0x41a000
	s_addc_u32 s25, s13, 0
	s_add_u32 s24, s24, s35
	s_addc_u32 s25, s25, 0
	s_add_u32 s26, s12, 0x1a000
	s_addc_u32 s27, s13, 0
	v_readfirstlane_b32 s3, v0
	s_cmp_lt_u32 s3, 64
	s_cbranch_scc0 .Lp2_polled
	s_mov_b32 s34, 0
	s_mov_b64 s[22:23], exec
	s_mov_b64 exec, 1
	s_and_b32 s3, s33, 31
	s_lshl_b32 s3, s3, 6
	s_add_u32 s3, s3, 4
	v_mov_b32_e32 v17, s3
